# baseline (speedup 1.0000x reference)
.LBB0_26:
	v_and_b32_e32 v2, 63, v0
	v_lshrrev_b32_e32 v3, 6, v0
	v_lshrrev_b32_e32 v4, 3, v2
	v_lshlrev_b32_e32 v4, 6, v4
	v_lshl_or_b32 v4, v3, 4, v4
	v_and_b32_e32 v6, 7, v2
	v_lshl_or_b32 v4, v6, 1, v4
	s_mov_b32 s0, 0x41800000
	v_fma_mixlo_f16 v16, v51, s0, 0
	v_fma_mixlo_f16 v20, v50, s0, 0
	v_fma_mixlo_f16 v17, v49, s0, 0
	v_fma_mixlo_f16 v21, v48, s0, 0
	v_fma_mixlo_f16 v18, v47, s0, 0
	v_fma_mixlo_f16 v22, v46, s0, 0
	v_fma_mixlo_f16 v19, v45, s0, 0
	v_fma_mixlo_f16 v23, v5, s0, 0
	ds_write_b16 v4, v16 offset:4096
	ds_write_b16 v4, v20 offset:6144
	ds_write_b16 v4, v17 offset:4608
	ds_write_b16 v4, v21 offset:6656
	ds_write_b16 v4, v18 offset:5120
	ds_write_b16 v4, v22 offset:7168
	ds_write_b16 v4, v19 offset:5632
	ds_write_b16 v4, v23 offset:7680
	v_lshlrev_b32_e32 v7, 4, v2
	v_lshl_or_b32 v7, v3, 10, v7
	v_lshrrev_b32_e32 v12, 2, v2
	v_lshl_or_b32 v12, v3, 4, v12
	v_lshlrev_b32_e32 v12, 15, v12
	v_sub_u32_e32 v13, v1, v3
	v_and_b32_e32 v14, 3, v2
	v_add_u32_e32 v13, v13, v14
	v_lshl_add_u32 v12, v13, 4, v12
	s_waitcnt lgkmcnt(0)
	s_barrier
	ds_read_b128 v[8:11], v7 offset:4096
	s_waitcnt lgkmcnt(0)
	global_store_dwordx4 v12, v[8:11], s[12:13] sc0 sc1
	s_endpgm
